# layer-0 gather: next-norm weights loaded once per layer instead of per token; the token epilogue's full wait removed
# baseline (speedup 1.0000x reference)
.Lgprio_l:
	v_add_u32_e32 v0, s6, v0
	v_cmp_gt_i32_e32 vcc, s87, v0
	s_and_saveexec_b64 s[6:7], vcc
	s_mov_b32 s12, 0x800000
	s_cbranch_execz .LBB0_772
	v_ashrrev_i32_e32 v1, 31, v0
	v_and_b32_e32 v2, 15, v3
	v_lshlrev_b64 v[4:5], 9, v[0:1]
	v_lshl_add_u64 v[8:9], s[94:95], 0, v[4:5]
	v_lshlrev_b32_e32 v144, 2, v2
	v_lshl_add_u64 v[8:9], v[8:9], 0, v[144:145]
	global_load_dword v96, v[8:9], off
	global_load_dword v122, v[8:9], off offset:64
	v_and_b32_e32 v6, 63, v3
	v_readlane_b32 s10, v253, 27
	v_lshlrev_b32_e32 v144, 3, v6
	v_readlane_b32 s11, v253, 28
	s_load_dwordx2 s[8:9], s[8:9], 0x10
	v_and_b32_e32 v1, 32, v3
	v_lshl_add_u64 v[16:17], s[10:11], 0, v[144:145]
	v_readlane_b32 s10, v253, 29
	v_readlane_b32 s11, v253, 30
	v_cmp_eq_u32_e64 s[40:41], 0, v1
	v_and_b32_e32 v1, 16, v3
	v_lshl_add_u64 v[18:19], s[10:11], 0, v[144:145]
	v_lshlrev_b32_e32 v144, 5, v6
	v_and_b32_e32 v97, 60, v3
	v_cmp_eq_u32_e64 s[42:43], 0, v1
	v_and_b32_e32 v1, 8, v3
	v_cmp_eq_u32_e64 s[44:45], 0, v1
	v_and_b32_e32 v1, 4, v3
	v_or_b32_e32 v4, v4, v97
	v_cmp_eq_u32_e64 s[46:47], 0, v1
	s_waitcnt vmcnt(0)
	v_readlane_b32 s10, v96, 0
	s_ashr_i32 s11, s10, 31
	s_lshl_b64 s[10:11], s[10:11], 9
	v_lshl_add_u64 v[8:9], v[16:17], 0, s[10:11]
	global_load_dwordx2 v[20:21], v[8:9], off
	v_lshl_add_u64 v[8:9], v[18:19], 0, s[10:11]
	v_readlane_b32 s10, v96, 1
	s_ashr_i32 s11, s10, 31
	s_lshl_b64 s[10:11], s[10:11], 9
	global_load_dwordx2 v[92:93], v[8:9], off
	v_lshl_add_u64 v[8:9], v[16:17], 0, s[10:11]
	global_load_dwordx2 v[22:23], v[8:9], off
	v_lshl_add_u64 v[8:9], v[18:19], 0, s[10:11]
	v_readlane_b32 s10, v96, 2
	s_ashr_i32 s11, s10, 31
	s_lshl_b64 s[10:11], s[10:11], 9
	global_load_dwordx2 v[90:91], v[8:9], off
	v_lshl_add_u64 v[8:9], v[16:17], 0, s[10:11]
	global_load_dwordx2 v[24:25], v[8:9], off
	v_lshl_add_u64 v[8:9], v[18:19], 0, s[10:11]
	v_readlane_b32 s10, v96, 3
	s_ashr_i32 s11, s10, 31
	s_lshl_b64 s[10:11], s[10:11], 9
	global_load_dwordx2 v[88:89], v[8:9], off
	v_lshl_add_u64 v[8:9], v[16:17], 0, s[10:11]
	global_load_dwordx2 v[26:27], v[8:9], off
	v_lshl_add_u64 v[8:9], v[18:19], 0, s[10:11]
	v_readlane_b32 s10, v96, 4
	s_ashr_i32 s11, s10, 31
	s_lshl_b64 s[10:11], s[10:11], 9
	global_load_dwordx2 v[86:87], v[8:9], off
	v_lshl_add_u64 v[8:9], v[16:17], 0, s[10:11]
	global_load_dwordx2 v[28:29], v[8:9], off
	v_lshl_add_u64 v[8:9], v[18:19], 0, s[10:11]
	v_readlane_b32 s10, v96, 5
	s_ashr_i32 s11, s10, 31
	s_lshl_b64 s[10:11], s[10:11], 9
	global_load_dwordx2 v[84:85], v[8:9], off
	v_lshl_add_u64 v[8:9], v[16:17], 0, s[10:11]
	global_load_dwordx2 v[30:31], v[8:9], off
	v_lshl_add_u64 v[8:9], v[18:19], 0, s[10:11]
	v_readlane_b32 s10, v96, 6
	s_ashr_i32 s11, s10, 31
	s_lshl_b64 s[10:11], s[10:11], 9
	global_load_dwordx2 v[82:83], v[8:9], off
	v_lshl_add_u64 v[8:9], v[16:17], 0, s[10:11]
	global_load_dwordx2 v[32:33], v[8:9], off
	v_lshl_add_u64 v[8:9], v[18:19], 0, s[10:11]
	v_readlane_b32 s10, v96, 7
	s_ashr_i32 s11, s10, 31
	s_lshl_b64 s[10:11], s[10:11], 9
	global_load_dwordx2 v[80:81], v[8:9], off
	v_lshl_add_u64 v[8:9], v[16:17], 0, s[10:11]
	global_load_dwordx2 v[34:35], v[8:9], off
	v_lshl_add_u64 v[8:9], v[18:19], 0, s[10:11]
	v_readlane_b32 s10, v96, 8
	s_ashr_i32 s11, s10, 31
	s_lshl_b64 s[10:11], s[10:11], 9
	global_load_dwordx2 v[78:79], v[8:9], off
	v_lshl_add_u64 v[8:9], v[16:17], 0, s[10:11]
	global_load_dwordx2 v[36:37], v[8:9], off
	v_lshl_add_u64 v[8:9], v[18:19], 0, s[10:11]
	v_readlane_b32 s10, v96, 9
	s_ashr_i32 s11, s10, 31
	s_lshl_b64 s[10:11], s[10:11], 9
	global_load_dwordx2 v[76:77], v[8:9], off
	v_lshl_add_u64 v[8:9], v[16:17], 0, s[10:11]
	global_load_dwordx2 v[38:39], v[8:9], off
	v_lshl_add_u64 v[8:9], v[18:19], 0, s[10:11]
	v_readlane_b32 s10, v96, 10
	s_ashr_i32 s11, s10, 31
	s_lshl_b64 s[10:11], s[10:11], 9
	global_load_dwordx2 v[70:71], v[8:9], off
	v_lshl_add_u64 v[8:9], v[16:17], 0, s[10:11]
	global_load_dwordx2 v[40:41], v[8:9], off
	v_lshl_add_u64 v[8:9], v[18:19], 0, s[10:11]
	v_readlane_b32 s10, v96, 11
	s_ashr_i32 s11, s10, 31
	s_lshl_b64 s[10:11], s[10:11], 9
	global_load_dwordx2 v[66:67], v[8:9], off
	v_lshl_add_u64 v[8:9], v[16:17], 0, s[10:11]
	global_load_dwordx2 v[60:61], v[8:9], off
	v_lshl_add_u64 v[8:9], v[18:19], 0, s[10:11]
	v_readlane_b32 s10, v96, 12
	s_ashr_i32 s11, s10, 31
	s_lshl_b64 s[10:11], s[10:11], 9
	global_load_dwordx2 v[72:73], v[8:9], off
	v_lshl_add_u64 v[8:9], v[16:17], 0, s[10:11]
	global_load_dwordx2 v[58:59], v[8:9], off
	v_lshl_add_u64 v[8:9], v[18:19], 0, s[10:11]
	v_readlane_b32 s10, v96, 13
	s_ashr_i32 s11, s10, 31
	s_lshl_b64 s[10:11], s[10:11], 9
	global_load_dwordx2 v[68:69], v[8:9], off
	v_lshl_add_u64 v[8:9], v[16:17], 0, s[10:11]
	global_load_dwordx2 v[56:57], v[8:9], off
	v_lshl_add_u64 v[8:9], v[18:19], 0, s[10:11]
	v_readlane_b32 s10, v96, 14
	s_ashr_i32 s11, s10, 31
	s_lshl_b64 s[10:11], s[10:11], 9
	global_load_dwordx2 v[64:65], v[8:9], off
	v_lshl_add_u64 v[8:9], v[16:17], 0, s[10:11]
	global_load_dwordx2 v[54:55], v[8:9], off
	v_lshl_add_u64 v[8:9], v[18:19], 0, s[10:11]
	v_readlane_b32 s10, v96, 15
	s_ashr_i32 s11, s10, 31
	s_lshl_b64 s[10:11], s[10:11], 9
	global_load_dwordx2 v[62:63], v[8:9], off
	v_lshl_add_u64 v[8:9], v[16:17], 0, s[10:11]
	global_load_dwordx2 v[52:53], v[8:9], off
	v_lshl_add_u64 v[8:9], v[18:19], 0, s[10:11]
	global_load_dwordx2 v[50:51], v[8:9], off
	v_readlane_b32 s10, v253, 15
	v_readlane_b32 s11, v253, 16
	s_nop 1
	v_lshl_add_u64 v[42:43], s[10:11], 0, v[144:145]
	v_lshlrev_b32_e32 v144, 6, v6
	s_waitcnt lgkmcnt(0)
	v_lshl_add_u64 v[6:7], s[8:9], 0, v[144:145]
	s_mov_b64 s[8:9], 0x1000
	v_readlane_b32 s10, v253, 13
	v_lshl_add_u64 v[46:47], v[6:7], 0, s[8:9]
	v_readlane_b32 s8, v253, 23
	v_readlane_b32 s11, v253, 14
	v_readlane_b32 s9, v253, 24
	s_nop 0
	v_lshl_add_u64 v[44:45], s[10:11], 0, v[144:145]
	v_lshl_add_u64 v[48:49], s[8:9], 0, v[4:5]
	s_mov_b64 s[8:9], 0
	v_lshlrev_b32_e32 v144, 2, v2
	v_readfirstlane_b32 s62, v16
	v_readfirstlane_b32 s63, v17
	v_readfirstlane_b32 s64, v18
	v_readfirstlane_b32 s65, v19
	v_and_b32_e32 v121, 63, v175
	v_lshlrev_b32_e32 v121, 3, v121
	global_load_dwordx4 v[124:127], v[46:47], off
	global_load_dwordx4 v[128:131], v[46:47], off offset:16
	global_load_dwordx4 v[132:135], v[46:47], off offset:32
	global_load_dwordx4 v[136:139], v[46:47], off offset:48
	v_mov_b32_e32 v250, v0
	v_ashrrev_i32_e32 v251, 31, v250
	v_lshlrev_b64 v[250:251], 6, v[250:251]
	v_lshl_add_u64 v[16:17], s[96:97], 0, v[250:251]
	v_lshlrev_b64 v[250:251], 5, v[250:251]
	v_lshl_add_u64 v[250:251], v[42:43], 0, v[250:251]
	global_load_dwordx4 v[226:229], v[16:17], off
	global_load_dwordx4 v[230:233], v[16:17], off offset:16
	global_load_dwordx4 v[234:237], v[16:17], off offset:32
	global_load_dwordx4 v[238:241], v[250:251], off
	global_load_dwordx4 v[242:245], v[250:251], off offset:16
	global_load_dwordx4 v[246:249], v[16:17], off offset:48
	s_waitcnt vmcnt(0)

.LBB0_770:
	s_cmpk_ge_i32 s56, 0x70
	s_cselect_b64 s[10:11], -1, 0
	ds_bpermute_b32 v6, v97, v96
	s_and_b64 vcc, s[10:11], s[48:49]
	v_cndmask_b32_e32 v94, v0, v98, vcc
	v_ashrrev_i32_e32 v95, 31, v94
	s_add_i32 s10, s56, 16
	s_and_b32 s10, s10, 0x70
	v_lshlrev_b64 v[94:95], 9, v[94:95]
	v_lshl_add_u64 v[94:95], s[94:95], 0, v[94:95]
	s_lshl_b32 s36, s10, 2
	s_waitcnt lgkmcnt(0)
	s_waitcnt vmcnt(32)
	v_mov_b32_e32 v96, v122
	v_ashrrev_i32_e32 v7, 31, v6
	v_lshl_add_u64 v[94:95], v[94:95], 0, s[36:37]
	v_lshl_add_u64 v[6:7], v[6:7], 3, s[88:89]
	v_lshl_add_u64 v[94:95], v[94:95], 0, v[144:145]
	global_load_dwordx2 v[6:7], v[6:7], off
	s_nop 0
	global_load_dword v8, v[4:5], off
	global_load_dword v122, v[94:95], off
	s_waitcnt vmcnt(19)
	v_dot8_i32_i4 v9, v20, v1, 0
	v_dot8_i32_i4 v94, v20, v10, 0
	v_dot8_i32_i4 v9, v21, v11, v9
	v_dot8_i32_i4 v94, v21, v12, v94
	v_dot8_i32_i4 v20, v22, v1, 0
	v_dot8_i32_i4 v21, v22, v10, 0
	v_dot8_i32_i4 v20, v23, v11, v20
	v_dot8_i32_i4 v21, v23, v12, v21
	v_lshl_add_u32 v9, v9, 4, v94
	s_add_i32 s56, s56, 16
	s_nop 0
	v_lshl_add_u32 v94, v20, 4, v21
	s_waitcnt vmcnt(19)
	v_dot8_i32_i4 v20, v24, v1, 0
	v_dot8_i32_i4 v21, v24, v10, 0
	v_dot8_i32_i4 v20, v25, v11, v20
	v_dot8_i32_i4 v21, v25, v12, v21
	v_lshl_add_u64 v[4:5], v[4:5], 0, 64
	s_nop 1
	v_lshl_add_u32 v95, v20, 4, v21
	v_dot8_i32_i4 v20, v26, v1, 0
	v_dot8_i32_i4 v21, v26, v10, 0
	v_dot8_i32_i4 v20, v27, v11, v20
	v_dot8_i32_i4 v21, v27, v12, v21
	v_readlane_b32 s10, v96, 0
	s_ashr_i32 s11, s10, 31
	v_readlane_b32 s12, v96, 1
	v_lshl_add_u32 v106, v20, 4, v21
	v_dot8_i32_i4 v20, v28, v1, 0
	v_dot8_i32_i4 v21, v28, v10, 0
	v_dot8_i32_i4 v20, v29, v11, v20
	v_dot8_i32_i4 v21, v29, v12, v21
	s_lshl_b64 s[10:11], s[10:11], 9
	s_ashr_i32 s13, s12, 31
	v_readlane_b32 s14, v96, 2
	v_lshl_add_u32 v107, v20, 4, v21
	v_dot8_i32_i4 v20, v30, v1, 0
	v_dot8_i32_i4 v21, v30, v10, 0
	v_dot8_i32_i4 v20, v31, v11, v20
	v_dot8_i32_i4 v21, v31, v12, v21
	s_lshl_b64 s[12:13], s[12:13], 9
	s_ashr_i32 s15, s14, 31
	v_readlane_b32 s16, v96, 3
	v_lshl_add_u32 v108, v20, 4, v21
	v_dot8_i32_i4 v20, v32, v1, 0
	v_dot8_i32_i4 v21, v32, v10, 0
	v_dot8_i32_i4 v20, v33, v11, v20
	v_dot8_i32_i4 v21, v33, v12, v21
	s_lshl_b64 s[14:15], s[14:15], 9
	s_ashr_i32 s17, s16, 31
	s_nop 0
	v_lshl_add_u32 v109, v20, 4, v21
	v_dot8_i32_i4 v20, v34, v1, 0
	v_dot8_i32_i4 v21, v34, v10, 0
	v_dot8_i32_i4 v20, v35, v11, v20
	v_dot8_i32_i4 v21, v35, v12, v21
	v_readlane_b32 s18, v96, 4
	s_add_u32 s66, s12, s62
	s_addc_u32 s67, s13, s63
	global_load_dwordx2 v[22:23], v121, s[66:67]
	v_lshl_add_u32 v110, v20, 4, v21
	v_dot8_i32_i4 v20, v36, v1, 0
	v_dot8_i32_i4 v21, v36, v10, 0
	v_dot8_i32_i4 v20, v37, v11, v20
	v_dot8_i32_i4 v21, v37, v12, v21
	s_lshl_b64 s[16:17], s[16:17], 9
	s_ashr_i32 s19, s18, 31
	v_readlane_b32 s20, v96, 5
	v_lshl_add_u32 v111, v20, 4, v21
	v_dot8_i32_i4 v20, v38, v1, 0
	v_dot8_i32_i4 v21, v38, v10, 0
	v_dot8_i32_i4 v20, v39, v11, v20
	v_dot8_i32_i4 v21, v39, v12, v21
	s_setprio 2
	v_permlane32_swap_b32 v9, v111
	s_nop 1
	v_lshl_add_u32 v112, v20, 4, v21
	v_dot8_i32_i4 v20, v40, v1, 0
	v_dot8_i32_i4 v21, v40, v10, 0
	v_dot8_i32_i4 v20, v41, v11, v20
	v_dot8_i32_i4 v21, v41, v12, v21
	s_waitcnt lgkmcnt(0)
	v_add_u32_e32 v9, v9, v111
	v_permlane32_swap_b32 v94, v112
	v_lshl_add_u32 v113, v20, 4, v21
	v_dot8_i32_i4 v20, v60, v1, 0
	v_dot8_i32_i4 v21, v60, v10, 0
	v_dot8_i32_i4 v20, v61, v11, v20
	v_dot8_i32_i4 v21, v61, v12, v21
	s_waitcnt lgkmcnt(0)
	v_add_u32_e32 v94, v94, v112
	v_permlane32_swap_b32 v95, v113
	v_lshl_add_u32 v114, v20, 4, v21
	v_dot8_i32_i4 v20, v58, v1, 0
	v_dot8_i32_i4 v21, v58, v10, 0
	v_dot8_i32_i4 v20, v59, v11, v20
	v_dot8_i32_i4 v21, v59, v12, v21
	s_waitcnt lgkmcnt(0)
	v_add_u32_e32 v95, v95, v113
	v_permlane32_swap_b32 v106, v114
	v_lshl_add_u32 v115, v20, 4, v21
	v_dot8_i32_i4 v20, v56, v1, 0
	v_dot8_i32_i4 v21, v56, v10, 0
	v_dot8_i32_i4 v20, v57, v11, v20
	v_dot8_i32_i4 v21, v57, v12, v21
	s_waitcnt lgkmcnt(0)
	v_add_u32_e32 v106, v106, v114
	v_permlane32_swap_b32 v107, v115
	v_lshl_add_u32 v116, v20, 4, v21
	v_dot8_i32_i4 v20, v54, v1, 0
	v_dot8_i32_i4 v21, v54, v10, 0
	v_dot8_i32_i4 v20, v55, v11, v20
	v_dot8_i32_i4 v21, v55, v12, v21
	s_waitcnt lgkmcnt(0)
	v_add_u32_e32 v107, v107, v115
	v_permlane32_swap_b32 v108, v116
	v_lshl_add_u32 v117, v20, 4, v21
	v_dot8_i32_i4 v20, v52, v1, 0
	v_dot8_i32_i4 v21, v52, v10, 0
	v_dot8_i32_i4 v20, v53, v11, v20
	v_dot8_i32_i4 v21, v53, v12, v21
	s_waitcnt lgkmcnt(0)
	v_add_u32_e32 v108, v108, v116
	v_permlane32_swap_b32 v109, v117
	v_lshl_add_u32 v118, v20, 4, v21
	s_waitcnt lgkmcnt(0)
	v_add_u32_e32 v109, v109, v117
	v_permlane32_swap_b32 v110, v118
	s_add_u32 s66, s10, s62
	s_addc_u32 s67, s11, s63
	global_load_dwordx2 v[20:21], v121, s[66:67]
	s_add_u32 s66, s14, s62
	s_addc_u32 s67, s15, s63
	global_load_dwordx2 v[24:25], v121, s[66:67]
	s_waitcnt lgkmcnt(0)
	v_add_u32_e32 v110, v110, v118
	v_permlane16_swap_b32 v9, v107
	s_lshl_b64 s[18:19], s[18:19], 9
	s_ashr_i32 s21, s20, 31
	v_readlane_b32 s22, v96, 6
	s_add_u32 s66, s16, s62
	s_addc_u32 s67, s17, s63
	global_load_dwordx2 v[26:27], v121, s[66:67]
	s_waitcnt lgkmcnt(0)
	v_add_u32_e32 v9, v9, v107
	v_permlane16_swap_b32 v94, v108
	s_lshl_b64 s[20:21], s[20:21], 9
	s_ashr_i32 s23, s22, 31
	s_waitcnt lgkmcnt(0)
	v_add_u32_e32 v94, v94, v108
	v_permlane16_swap_b32 v95, v109
	v_readlane_b32 s24, v96, 7
	s_add_u32 s66, s18, s62
	s_addc_u32 s67, s19, s63
	global_load_dwordx2 v[28:29], v121, s[66:67]
	s_waitcnt lgkmcnt(0)
	v_add_u32_e32 v95, v95, v109
	v_permlane16_swap_b32 v106, v110
	s_lshl_b64 s[22:23], s[22:23], 9
	s_ashr_i32 s25, s24, 31
	v_readlane_b32 s26, v96, 8
	s_waitcnt lgkmcnt(0)
	v_add_u32_e32 v106, v106, v110
	v_cndmask_b32_e64 v107, v9, v95, s[44:45]
	v_cndmask_b32_e64 v9, v95, v9, s[44:45]
	s_nop 0
	s_add_u32 s66, s20, s62
	s_addc_u32 s67, s21, s63
	global_load_dwordx2 v[30:31], v121, s[66:67]
	s_lshl_b64 s[24:25], s[24:25], 9
	s_ashr_i32 s27, s26, 31
	s_waitcnt lgkmcnt(0)
	v_add_u32_dpp v9, v107, v9 row_ror:8 row_mask:0xf bank_mask:0xf
	v_cndmask_b32_e64 v95, v94, v106, s[44:45]
	s_nop 1
	v_cndmask_b32_e64 v94, v106, v94, s[44:45]
	v_readlane_b32 s28, v96, 9
	s_add_u32 s66, s22, s62
	s_addc_u32 s67, s23, s63
	global_load_dwordx2 v[32:33], v121, s[66:67]
	s_waitcnt lgkmcnt(0)
	v_add_u32_dpp v94, v95, v94 row_ror:8 row_mask:0xf bank_mask:0xf
	v_cndmask_b32_e64 v95, v9, v94, s[46:47]
	v_cndmask_b32_e64 v9, v94, v9, s[46:47]
	s_nop 0
	v_mov_b32_dpp v94, v95 row_half_mirror row_mask:0xf bank_mask:0xf
	s_nop 1
	s_lshl_b64 s[26:27], s[26:27], 9
	s_ashr_i32 s29, s28, 31
	v_readlane_b32 s30, v96, 10
	s_add_u32 s66, s24, s62
	s_addc_u32 s67, s25, s63
	global_load_dwordx2 v[34:35], v121, s[66:67]
	s_waitcnt lgkmcnt(0)
	v_add_u32_dpp v9, v94, v9 quad_perm:[3,2,1,0] row_mask:0xf bank_mask:0xf
	s_nop 1
	s_lshl_b64 s[28:29], s[28:29], 9
	s_ashr_i32 s31, s30, 31
	v_readlane_b32 s34, v96, 11
	s_waitcnt lgkmcnt(0)
	v_add_u32_dpp v9, v9, v9 quad_perm:[2,3,0,1] row_mask:0xf bank_mask:0xf
	s_nop 1
	s_add_u32 s66, s26, s62
	s_addc_u32 s67, s27, s63
	global_load_dwordx2 v[36:37], v121, s[66:67]
	s_lshl_b64 s[30:31], s[30:31], 9
	s_ashr_i32 s35, s34, 31
	s_waitcnt lgkmcnt(0)
	v_add_u32_dpp v9, v9, v9 quad_perm:[1,0,3,2] row_mask:0xf bank_mask:0xf
	s_waitcnt vmcnt(10)
	v_mul_f32_e32 v7, v13, v7
	v_cvt_f32_i32_e32 v9, v9
	v_add_f32_e32 v9, v14, v9
	v_mul_f32_e32 v7, v7, v9
	v_mul_f32_e32 v9, 0x3d372713, v7
	v_mul_f32_e32 v9, v7, v9
	v_fma_f32 v9, v7, v9, v7
	v_mul_f32_e32 v9, 0x3fcc422a, v9
	v_mul_f32_e32 v9, 0xbfb8aa3b, v9
	v_exp_f32_e32 v9, v9
	v_readlane_b32 s38, v96, 12
	s_add_u32 s66, s28, s62
	s_addc_u32 s67, s29, s63
	global_load_dwordx2 v[38:39], v121, s[66:67]
	v_add_f32_e32 v9, 1.0, v9
	v_rcp_f32_e32 v9, v9
	s_lshl_b64 s[34:35], s[34:35], 9
	s_ashr_i32 s39, s38, 31
	s_lshl_b64 s[38:39], s[38:39], 9
	v_readlane_b32 s50, v96, 13
	v_readlane_b32 s52, v96, 14
	v_readlane_b32 s54, v96, 15
	s_ashr_i32 s51, s50, 31
	s_ashr_i32 s53, s52, 31
	s_ashr_i32 s55, s54, 31
	s_lshl_b64 s[50:51], s[50:51], 9
	s_lshl_b64 s[52:53], s[52:53], 9
	s_lshl_b64 s[54:55], s[54:55], 9
	s_add_u32 s66, s30, s62
	s_addc_u32 s67, s31, s63
	global_load_dwordx2 v[40:41], v121, s[66:67]
	s_add_u32 s66, s34, s62
	s_addc_u32 s67, s35, s63
	global_load_dwordx2 v[60:61], v121, s[66:67]
	s_add_u32 s66, s38, s62
	s_addc_u32 s67, s39, s63
	global_load_dwordx2 v[58:59], v121, s[66:67]
	s_add_u32 s66, s50, s62
	s_addc_u32 s67, s51, s63
	global_load_dwordx2 v[56:57], v121, s[66:67]
	s_add_u32 s66, s52, s62
	s_addc_u32 s67, s53, s63
	global_load_dwordx2 v[54:55], v121, s[66:67]
	s_add_u32 s66, s54, s62
	s_addc_u32 s67, s55, s63
	global_load_dwordx2 v[52:53], v121, s[66:67]
	v_pk_mul_f32 v[6:7], v[6:7], v[8:9]
	s_waitcnt vmcnt(34)
	v_alignbit_b32 v224, v92, v92, 4
	v_pk_mul_f32 v[6:7], v[6:7], v[6:7] op_sel:[0,1] op_sel_hi:[1,0]
	v_cvt_f16_f32_e32 v120, v6
	s_setprio 0
	v_and_b32_e32 v8, 0x7070707, v92
	v_readlane_b32 s36, v120, 0
	v_and_b32_e32 v9, 0x7070707, v224
	v_perm_b32 v8, s2, v205, v8
	v_perm_b32 v9, s2, v205, v9
	v_and_or_b32 v8, v92, s4, v8
	v_and_or_b32 v9, v224, s4, v9
	v_perm_b32 v92, v9, v8, s5
	v_perm_b32 v94, v9, v8, s33
	v_perm_b32 v95, v9, v8, s0
	v_perm_b32 v8, v9, v8, s1
	v_pk_fma_f16 v8, v8, s36, v102 op_sel_hi:[1,0,1]
	v_alignbit_b32 v225, v93, v93, 4
	v_pk_fma_f16 v9, v92, s36, v105 op_sel_hi:[1,0,1]
	v_pk_fma_f16 v92, v94, s36, v104 op_sel_hi:[1,0,1]
	v_pk_fma_f16 v94, v95, s36, v103 op_sel_hi:[1,0,1]
	v_and_b32_e32 v95, 0x7070707, v93
	v_and_b32_e32 v102, 0x7070707, v225
	v_perm_b32 v95, s2, v205, v95
	v_perm_b32 v102, s2, v205, v102
	v_and_or_b32 v95, v93, s4, v95
	v_and_or_b32 v93, v225, s4, v102
	v_perm_b32 v102, v93, v95, s5
	v_perm_b32 v103, v93, v95, s33
	v_perm_b32 v104, v93, v95, s0
	v_perm_b32 v93, v93, v95, s1
	v_pk_fma_f16 v95, v102, s36, v101 op_sel_hi:[1,0,1]
	v_readlane_b32 s59, v120, 4
	s_waitcnt vmcnt(33)
	v_alignbit_b32 v224, v90, v90, 4
	v_pk_fma_f16 v100, v103, s36, v100 op_sel_hi:[1,0,1]
	v_pk_fma_f16 v99, v104, s36, v99 op_sel_hi:[1,0,1]
	v_pk_fma_f16 v7, v93, s36, v15 op_sel_hi:[1,0,1]
	v_and_b32_e32 v93, 0x7070707, v90
	v_and_b32_e32 v101, 0x7070707, v224
	v_perm_b32 v93, s2, v205, v93
	v_perm_b32 v101, s2, v205, v101
	v_and_or_b32 v93, v90, s4, v93
	v_and_or_b32 v90, v224, s4, v101
	v_perm_b32 v103, v90, v93, s0
	v_perm_b32 v101, v90, v93, s5
	v_perm_b32 v102, v90, v93, s33
	v_perm_b32 v90, v90, v93, s1
	v_pk_fma_f16 v93, v103, s59, v94 op_sel_hi:[1,0,1]
	v_alignbit_b32 v225, v91, v91, 4
	v_pk_fma_f16 v8, v90, s59, v8 op_sel_hi:[1,0,1]
	v_and_b32_e32 v90, 0x7070707, v91
	v_and_b32_e32 v94, 0x7070707, v225
	v_pk_fma_f16 v9, v101, s59, v9 op_sel_hi:[1,0,1]
	v_perm_b32 v90, s2, v205, v90
	v_perm_b32 v94, s2, v205, v94
	v_and_or_b32 v90, v91, s4, v90
	v_and_or_b32 v91, v225, s4, v94
	v_pk_fma_f16 v92, v102, s59, v92 op_sel_hi:[1,0,1]
	v_perm_b32 v94, v91, v90, s5
	v_perm_b32 v102, v91, v90, s0
	v_perm_b32 v101, v91, v90, s33
	v_perm_b32 v90, v91, v90, s1
	v_pk_fma_f16 v91, v94, s59, v95 op_sel_hi:[1,0,1]
	v_pk_fma_f16 v95, v102, s59, v99 op_sel_hi:[1,0,1]
	v_readlane_b32 s60, v120, 8
	s_waitcnt vmcnt(32)
	v_alignbit_b32 v224, v88, v88, 4
	v_pk_fma_f16 v94, v101, s59, v100 op_sel_hi:[1,0,1]
	v_pk_fma_f16 v7, v90, s59, v7 op_sel_hi:[1,0,1]
	v_and_b32_e32 v90, 0x7070707, v88
	v_and_b32_e32 v99, 0x7070707, v224
	v_perm_b32 v90, s2, v205, v90
	v_perm_b32 v99, s2, v205, v99
	v_and_or_b32 v90, v88, s4, v90
	v_and_or_b32 v88, v224, s4, v99
	v_perm_b32 v100, v88, v90, s33
	v_perm_b32 v101, v88, v90, s0
	v_perm_b32 v99, v88, v90, s5
	v_perm_b32 v88, v88, v90, s1
	v_pk_fma_f16 v90, v100, s60, v92 op_sel_hi:[1,0,1]
	v_pk_fma_f16 v92, v101, s60, v93 op_sel_hi:[1,0,1]
	v_alignbit_b32 v225, v89, v89, 4
	v_pk_fma_f16 v8, v88, s60, v8 op_sel_hi:[1,0,1]
	v_and_b32_e32 v88, 0x7070707, v89
	v_and_b32_e32 v93, 0x7070707, v225
	v_pk_fma_f16 v9, v99, s60, v9 op_sel_hi:[1,0,1]
	v_perm_b32 v88, s2, v205, v88
	v_perm_b32 v93, s2, v205, v93
	v_and_or_b32 v88, v89, s4, v88
	v_and_or_b32 v89, v225, s4, v93
	v_perm_b32 v93, v89, v88, s5
	v_perm_b32 v99, v89, v88, s33
	v_perm_b32 v100, v89, v88, s0
	v_perm_b32 v88, v89, v88, s1
	v_pk_fma_f16 v89, v93, s60, v91 op_sel_hi:[1,0,1]
	v_pk_fma_f16 v91, v99, s60, v94 op_sel_hi:[1,0,1]
	v_readlane_b32 s36, v120, 12
	s_waitcnt vmcnt(31)
	v_alignbit_b32 v224, v86, v86, 4
	v_pk_fma_f16 v93, v100, s60, v95 op_sel_hi:[1,0,1]
	v_pk_fma_f16 v7, v88, s60, v7 op_sel_hi:[1,0,1]
	v_and_b32_e32 v88, 0x7070707, v86
	v_and_b32_e32 v94, 0x7070707, v224
	v_perm_b32 v88, s2, v205, v88
	v_perm_b32 v94, s2, v205, v94
	v_and_or_b32 v88, v86, s4, v88
	v_and_or_b32 v86, v224, s4, v94
	v_perm_b32 v95, v86, v88, s33
	v_perm_b32 v99, v86, v88, s0
	v_perm_b32 v94, v86, v88, s5
	v_perm_b32 v86, v86, v88, s1
	v_pk_fma_f16 v88, v95, s36, v90 op_sel_hi:[1,0,1]
	v_pk_fma_f16 v90, v99, s36, v92 op_sel_hi:[1,0,1]
	v_alignbit_b32 v225, v87, v87, 4
	v_pk_fma_f16 v8, v86, s36, v8 op_sel_hi:[1,0,1]
	v_and_b32_e32 v86, 0x7070707, v87
	v_and_b32_e32 v92, 0x7070707, v225
	v_pk_fma_f16 v9, v94, s36, v9 op_sel_hi:[1,0,1]
	v_perm_b32 v86, s2, v205, v86
	v_perm_b32 v92, s2, v205, v92
	v_and_or_b32 v86, v87, s4, v86
	v_and_or_b32 v87, v225, s4, v92
	v_perm_b32 v92, v87, v86, s5
	v_perm_b32 v94, v87, v86, s33
	v_perm_b32 v95, v87, v86, s0
	v_perm_b32 v86, v87, v86, s1
	v_pk_fma_f16 v87, v92, s36, v89 op_sel_hi:[1,0,1]
	v_readlane_b32 s59, v120, 16
	s_waitcnt vmcnt(30)
	v_alignbit_b32 v224, v84, v84, 4
	v_pk_fma_f16 v89, v94, s36, v91 op_sel_hi:[1,0,1]
	v_pk_fma_f16 v91, v95, s36, v93 op_sel_hi:[1,0,1]
	v_pk_fma_f16 v7, v86, s36, v7 op_sel_hi:[1,0,1]
	v_and_b32_e32 v86, 0x7070707, v84
	v_and_b32_e32 v92, 0x7070707, v224
	v_perm_b32 v86, s2, v205, v86
	v_perm_b32 v92, s2, v205, v92
	v_and_or_b32 v86, v84, s4, v86
	v_and_or_b32 v84, v224, s4, v92
	v_perm_b32 v93, v84, v86, s33
	v_perm_b32 v94, v84, v86, s0
	v_perm_b32 v92, v84, v86, s5
	v_perm_b32 v84, v84, v86, s1
	v_pk_fma_f16 v86, v93, s59, v88 op_sel_hi:[1,0,1]
	v_pk_fma_f16 v88, v94, s59, v90 op_sel_hi:[1,0,1]
	v_alignbit_b32 v225, v85, v85, 4
	v_pk_fma_f16 v8, v84, s59, v8 op_sel_hi:[1,0,1]
	v_and_b32_e32 v84, 0x7070707, v85
	v_and_b32_e32 v90, 0x7070707, v225
	v_pk_fma_f16 v9, v92, s59, v9 op_sel_hi:[1,0,1]
	v_perm_b32 v84, s2, v205, v84
	v_perm_b32 v90, s2, v205, v90
	v_and_or_b32 v84, v85, s4, v84
	v_and_or_b32 v85, v225, s4, v90
	v_perm_b32 v90, v85, v84, s5
	v_perm_b32 v92, v85, v84, s33
	v_perm_b32 v93, v85, v84, s0
	v_perm_b32 v84, v85, v84, s1
	v_pk_fma_f16 v85, v90, s59, v87 op_sel_hi:[1,0,1]
	v_readlane_b32 s60, v120, 20
	s_waitcnt vmcnt(29)
	v_alignbit_b32 v224, v82, v82, 4
	v_pk_fma_f16 v87, v92, s59, v89 op_sel_hi:[1,0,1]
	v_pk_fma_f16 v89, v93, s59, v91 op_sel_hi:[1,0,1]
	v_pk_fma_f16 v7, v84, s59, v7 op_sel_hi:[1,0,1]
	v_and_b32_e32 v84, 0x7070707, v82
	v_and_b32_e32 v90, 0x7070707, v224
	v_perm_b32 v84, s2, v205, v84
	v_perm_b32 v90, s2, v205, v90
	v_and_or_b32 v84, v82, s4, v84
	v_and_or_b32 v82, v224, s4, v90
	v_perm_b32 v91, v82, v84, s33
	v_perm_b32 v92, v82, v84, s0
	v_perm_b32 v90, v82, v84, s5
	v_perm_b32 v82, v82, v84, s1
	v_pk_fma_f16 v84, v91, s60, v86 op_sel_hi:[1,0,1]
	v_pk_fma_f16 v86, v92, s60, v88 op_sel_hi:[1,0,1]
	s_add_u32 s66, s10, s64
	s_addc_u32 s67, s11, s65
	global_load_dwordx2 v[92:93], v121, s[66:67]
	v_alignbit_b32 v225, v83, v83, 4
	v_pk_fma_f16 v8, v82, s60, v8 op_sel_hi:[1,0,1]
	v_and_b32_e32 v82, 0x7070707, v83
	v_and_b32_e32 v88, 0x7070707, v225
	v_pk_fma_f16 v9, v90, s60, v9 op_sel_hi:[1,0,1]
	v_perm_b32 v82, s2, v205, v82
	v_perm_b32 v88, s2, v205, v88
	v_and_or_b32 v82, v83, s4, v82
	v_and_or_b32 v83, v225, s4, v88
	v_perm_b32 v88, v83, v82, s5
	v_perm_b32 v90, v83, v82, s33
	v_perm_b32 v91, v83, v82, s0
	v_perm_b32 v82, v83, v82, s1
	v_pk_fma_f16 v83, v88, s60, v85 op_sel_hi:[1,0,1]
	v_readlane_b32 s36, v120, 24
	s_waitcnt vmcnt(29)
	v_alignbit_b32 v224, v80, v80, 4
	v_pk_fma_f16 v85, v90, s60, v87 op_sel_hi:[1,0,1]
	v_pk_fma_f16 v87, v91, s60, v89 op_sel_hi:[1,0,1]
	v_pk_fma_f16 v7, v82, s60, v7 op_sel_hi:[1,0,1]
	v_and_b32_e32 v82, 0x7070707, v80
	v_and_b32_e32 v88, 0x7070707, v224
	v_perm_b32 v82, s2, v205, v82
	v_perm_b32 v88, s2, v205, v88
	v_and_or_b32 v82, v80, s4, v82
	v_and_or_b32 v80, v224, s4, v88
	v_perm_b32 v89, v80, v82, s33
	v_perm_b32 v90, v80, v82, s0
	v_perm_b32 v88, v80, v82, s5
	v_perm_b32 v80, v80, v82, s1
	v_pk_fma_f16 v82, v89, s36, v84 op_sel_hi:[1,0,1]
	v_pk_fma_f16 v84, v90, s36, v86 op_sel_hi:[1,0,1]
	s_add_u32 s66, s12, s64
	s_addc_u32 s67, s13, s65
	global_load_dwordx2 v[90:91], v121, s[66:67]
	v_alignbit_b32 v225, v81, v81, 4
	v_pk_fma_f16 v8, v80, s36, v8 op_sel_hi:[1,0,1]
	v_and_b32_e32 v80, 0x7070707, v81
	v_and_b32_e32 v86, 0x7070707, v225
	v_pk_fma_f16 v9, v88, s36, v9 op_sel_hi:[1,0,1]
	v_perm_b32 v80, s2, v205, v80
	v_perm_b32 v86, s2, v205, v86
	v_and_or_b32 v80, v81, s4, v80
	v_and_or_b32 v81, v225, s4, v86
	v_perm_b32 v86, v81, v80, s5
	v_perm_b32 v88, v81, v80, s33
	v_perm_b32 v89, v81, v80, s0
	v_perm_b32 v80, v81, v80, s1
	v_pk_fma_f16 v81, v86, s36, v83 op_sel_hi:[1,0,1]
	v_readlane_b32 s59, v120, 28
	s_waitcnt vmcnt(29)
	v_alignbit_b32 v224, v78, v78, 4
	v_pk_fma_f16 v83, v88, s36, v85 op_sel_hi:[1,0,1]
	v_pk_fma_f16 v85, v89, s36, v87 op_sel_hi:[1,0,1]
	v_pk_fma_f16 v7, v80, s36, v7 op_sel_hi:[1,0,1]
	v_and_b32_e32 v80, 0x7070707, v78
	v_and_b32_e32 v86, 0x7070707, v224
	v_perm_b32 v80, s2, v205, v80
	v_perm_b32 v86, s2, v205, v86
	v_and_or_b32 v80, v78, s4, v80
	v_and_or_b32 v78, v224, s4, v86
	v_perm_b32 v87, v78, v80, s33
	v_perm_b32 v88, v78, v80, s0
	v_perm_b32 v86, v78, v80, s5
	v_perm_b32 v78, v78, v80, s1
	v_pk_fma_f16 v80, v87, s59, v82 op_sel_hi:[1,0,1]
	v_pk_fma_f16 v82, v88, s59, v84 op_sel_hi:[1,0,1]
	s_add_u32 s66, s14, s64
	s_addc_u32 s67, s15, s65
	global_load_dwordx2 v[88:89], v121, s[66:67]
	v_alignbit_b32 v225, v79, v79, 4
	v_pk_fma_f16 v8, v78, s59, v8 op_sel_hi:[1,0,1]
	v_and_b32_e32 v78, 0x7070707, v79
	v_and_b32_e32 v84, 0x7070707, v225
	v_pk_fma_f16 v9, v86, s59, v9 op_sel_hi:[1,0,1]
	v_perm_b32 v78, s2, v205, v78
	v_perm_b32 v84, s2, v205, v84
	v_and_or_b32 v78, v79, s4, v78
	v_and_or_b32 v79, v225, s4, v84
	v_perm_b32 v84, v79, v78, s5
	v_perm_b32 v86, v79, v78, s33
	v_perm_b32 v87, v79, v78, s0
	v_perm_b32 v78, v79, v78, s1
	v_pk_fma_f16 v79, v84, s59, v81 op_sel_hi:[1,0,1]
	v_readlane_b32 s60, v120, 32
	s_waitcnt vmcnt(29)
	v_alignbit_b32 v224, v76, v76, 4
	v_pk_fma_f16 v81, v86, s59, v83 op_sel_hi:[1,0,1]
	v_pk_fma_f16 v83, v87, s59, v85 op_sel_hi:[1,0,1]
	v_pk_fma_f16 v7, v78, s59, v7 op_sel_hi:[1,0,1]
	v_and_b32_e32 v78, 0x7070707, v76
	v_and_b32_e32 v84, 0x7070707, v224
	v_perm_b32 v78, s2, v205, v78
	v_perm_b32 v84, s2, v205, v84
	v_and_or_b32 v78, v76, s4, v78
	v_and_or_b32 v76, v224, s4, v84
	v_perm_b32 v85, v76, v78, s33
	v_perm_b32 v86, v76, v78, s0
	v_perm_b32 v84, v76, v78, s5
	v_perm_b32 v76, v76, v78, s1
	v_pk_fma_f16 v78, v85, s60, v80 op_sel_hi:[1,0,1]
	v_pk_fma_f16 v80, v86, s60, v82 op_sel_hi:[1,0,1]
	s_add_u32 s66, s16, s64
	s_addc_u32 s67, s17, s65
	global_load_dwordx2 v[86:87], v121, s[66:67]
	v_alignbit_b32 v225, v77, v77, 4
	v_pk_fma_f16 v8, v76, s60, v8 op_sel_hi:[1,0,1]
	v_and_b32_e32 v76, 0x7070707, v77
	v_and_b32_e32 v82, 0x7070707, v225
	v_pk_fma_f16 v9, v84, s60, v9 op_sel_hi:[1,0,1]
	v_perm_b32 v76, s2, v205, v76
	v_perm_b32 v82, s2, v205, v82
	v_and_or_b32 v76, v77, s4, v76
	v_and_or_b32 v77, v225, s4, v82
	v_perm_b32 v82, v77, v76, s5
	v_perm_b32 v84, v77, v76, s33
	v_perm_b32 v85, v77, v76, s0
	v_perm_b32 v76, v77, v76, s1
	v_pk_fma_f16 v77, v82, s60, v79 op_sel_hi:[1,0,1]
	v_readlane_b32 s36, v120, 36
	s_waitcnt vmcnt(28)
	v_alignbit_b32 v224, v70, v70, 4
	v_pk_fma_f16 v79, v84, s60, v81 op_sel_hi:[1,0,1]
	v_pk_fma_f16 v81, v85, s60, v83 op_sel_hi:[1,0,1]
	v_pk_fma_f16 v7, v76, s60, v7 op_sel_hi:[1,0,1]
	v_and_b32_e32 v76, 0x7070707, v70
	v_and_b32_e32 v82, 0x7070707, v224
	v_perm_b32 v76, s2, v205, v76
	v_perm_b32 v82, s2, v205, v82
	v_and_or_b32 v76, v70, s4, v76
	v_and_or_b32 v70, v224, s4, v82
	v_perm_b32 v83, v70, v76, s33
	v_perm_b32 v84, v70, v76, s0
	v_perm_b32 v82, v70, v76, s5
	v_perm_b32 v70, v70, v76, s1
	v_pk_fma_f16 v76, v83, s36, v78 op_sel_hi:[1,0,1]
	v_pk_fma_f16 v78, v84, s36, v80 op_sel_hi:[1,0,1]
	s_add_u32 s66, s18, s64
	s_addc_u32 s67, s19, s65
	global_load_dwordx2 v[84:85], v121, s[66:67]
	v_alignbit_b32 v225, v71, v71, 4
	v_pk_fma_f16 v8, v70, s36, v8 op_sel_hi:[1,0,1]
	v_and_b32_e32 v70, 0x7070707, v71
	v_and_b32_e32 v80, 0x7070707, v225
	v_pk_fma_f16 v9, v82, s36, v9 op_sel_hi:[1,0,1]
	v_perm_b32 v70, s2, v205, v70
	v_perm_b32 v80, s2, v205, v80
	v_and_or_b32 v70, v71, s4, v70
	v_and_or_b32 v71, v225, s4, v80
	v_perm_b32 v80, v71, v70, s5
	v_perm_b32 v82, v71, v70, s33
	v_perm_b32 v83, v71, v70, s0
	v_perm_b32 v70, v71, v70, s1
	v_pk_fma_f16 v71, v80, s36, v77 op_sel_hi:[1,0,1]
	v_readlane_b32 s59, v120, 40
	s_waitcnt vmcnt(25)
	v_alignbit_b32 v224, v66, v66, 4
	v_pk_fma_f16 v77, v82, s36, v79 op_sel_hi:[1,0,1]
	v_pk_fma_f16 v79, v83, s36, v81 op_sel_hi:[1,0,1]
	v_pk_fma_f16 v7, v70, s36, v7 op_sel_hi:[1,0,1]
	v_and_b32_e32 v70, 0x7070707, v66
	v_and_b32_e32 v80, 0x7070707, v224
	v_perm_b32 v70, s2, v205, v70
	v_perm_b32 v80, s2, v205, v80
	v_and_or_b32 v70, v66, s4, v70
	v_and_or_b32 v66, v224, s4, v80
	v_perm_b32 v81, v66, v70, s33
	v_perm_b32 v82, v66, v70, s0
	v_perm_b32 v80, v66, v70, s5
	v_perm_b32 v66, v66, v70, s1
	v_pk_fma_f16 v70, v81, s59, v76 op_sel_hi:[1,0,1]
	v_pk_fma_f16 v76, v82, s59, v78 op_sel_hi:[1,0,1]
	s_add_u32 s66, s20, s64
	s_addc_u32 s67, s21, s65
	global_load_dwordx2 v[82:83], v121, s[66:67]
	v_alignbit_b32 v225, v67, v67, 4
	v_pk_fma_f16 v8, v66, s59, v8 op_sel_hi:[1,0,1]
	v_and_b32_e32 v66, 0x7070707, v67
	v_and_b32_e32 v78, 0x7070707, v225
	v_pk_fma_f16 v9, v80, s59, v9 op_sel_hi:[1,0,1]
	v_perm_b32 v66, s2, v205, v66
	v_perm_b32 v78, s2, v205, v78
	v_and_or_b32 v66, v67, s4, v66
	v_and_or_b32 v67, v225, s4, v78
	v_perm_b32 v78, v67, v66, s5
	v_perm_b32 v80, v67, v66, s33
	v_perm_b32 v81, v67, v66, s0
	v_perm_b32 v66, v67, v66, s1
	v_pk_fma_f16 v67, v78, s59, v71 op_sel_hi:[1,0,1]
	v_readlane_b32 s60, v120, 44
	s_waitcnt vmcnt(31)
	v_alignbit_b32 v224, v72, v72, 4
	v_pk_fma_f16 v71, v80, s59, v77 op_sel_hi:[1,0,1]
	v_pk_fma_f16 v77, v81, s59, v79 op_sel_hi:[1,0,1]
	v_pk_fma_f16 v7, v66, s59, v7 op_sel_hi:[1,0,1]
	v_and_b32_e32 v66, 0x7070707, v72
	v_and_b32_e32 v78, 0x7070707, v224
	v_perm_b32 v66, s2, v205, v66
	v_perm_b32 v78, s2, v205, v78
	v_and_or_b32 v66, v72, s4, v66
	v_and_or_b32 v72, v224, s4, v78
	v_perm_b32 v80, v72, v66, s0
	v_perm_b32 v78, v72, v66, s5
	v_perm_b32 v79, v72, v66, s33
	v_perm_b32 v66, v72, v66, s1
	v_pk_fma_f16 v72, v80, s60, v76 op_sel_hi:[1,0,1]
	s_add_u32 s66, s22, s64
	s_addc_u32 s67, s23, s65
	global_load_dwordx2 v[80:81], v121, s[66:67]
	v_alignbit_b32 v225, v73, v73, 4
	v_pk_fma_f16 v8, v66, s60, v8 op_sel_hi:[1,0,1]
	v_and_b32_e32 v66, 0x7070707, v73
	v_and_b32_e32 v76, 0x7070707, v225
	v_pk_fma_f16 v9, v78, s60, v9 op_sel_hi:[1,0,1]
	v_perm_b32 v66, s2, v205, v66
	v_perm_b32 v76, s2, v205, v76
	v_and_or_b32 v66, v73, s4, v66
	v_and_or_b32 v73, v225, s4, v76
	v_perm_b32 v76, v73, v66, s5
	v_pk_fma_f16 v70, v79, s60, v70 op_sel_hi:[1,0,1]
	v_perm_b32 v78, v73, v66, s33
	v_perm_b32 v79, v73, v66, s0
	v_perm_b32 v66, v73, v66, s1
	v_pk_fma_f16 v67, v76, s60, v67 op_sel_hi:[1,0,1]
	v_readlane_b32 s36, v120, 48
	s_waitcnt vmcnt(30)
	v_alignbit_b32 v224, v68, v68, 4
	v_pk_fma_f16 v71, v78, s60, v71 op_sel_hi:[1,0,1]
	v_pk_fma_f16 v73, v79, s60, v77 op_sel_hi:[1,0,1]
	v_pk_fma_f16 v7, v66, s60, v7 op_sel_hi:[1,0,1]
	v_and_b32_e32 v66, 0x7070707, v68
	v_and_b32_e32 v76, 0x7070707, v224
	v_perm_b32 v66, s2, v205, v66
	v_perm_b32 v76, s2, v205, v76
	v_and_or_b32 v66, v68, s4, v66
	v_and_or_b32 v68, v224, s4, v76
	v_perm_b32 v77, v68, v66, s33
	v_perm_b32 v78, v68, v66, s0
	v_perm_b32 v76, v68, v66, s5
	v_perm_b32 v66, v68, v66, s1
	v_pk_fma_f16 v68, v77, s36, v70 op_sel_hi:[1,0,1]
	v_pk_fma_f16 v70, v78, s36, v72 op_sel_hi:[1,0,1]
	s_add_u32 s66, s24, s64
	s_addc_u32 s67, s25, s65
	global_load_dwordx2 v[78:79], v121, s[66:67]
	v_alignbit_b32 v225, v69, v69, 4
	v_pk_fma_f16 v8, v66, s36, v8 op_sel_hi:[1,0,1]
	v_and_b32_e32 v66, 0x7070707, v69
	v_and_b32_e32 v72, 0x7070707, v225
	v_pk_fma_f16 v9, v76, s36, v9 op_sel_hi:[1,0,1]
	v_perm_b32 v66, s2, v205, v66
	v_perm_b32 v72, s2, v205, v72
	v_and_or_b32 v66, v69, s4, v66
	v_and_or_b32 v69, v225, s4, v72
	v_perm_b32 v72, v69, v66, s5
	v_perm_b32 v76, v69, v66, s33
	v_perm_b32 v77, v69, v66, s0
	v_perm_b32 v66, v69, v66, s1
	v_pk_fma_f16 v67, v72, s36, v67 op_sel_hi:[1,0,1]
	v_readlane_b32 s59, v120, 52
	s_waitcnt vmcnt(29)
	v_alignbit_b32 v224, v64, v64, 4
	v_pk_fma_f16 v69, v76, s36, v71 op_sel_hi:[1,0,1]
	v_pk_fma_f16 v71, v77, s36, v73 op_sel_hi:[1,0,1]
	v_pk_fma_f16 v7, v66, s36, v7 op_sel_hi:[1,0,1]
	v_and_b32_e32 v66, 0x7070707, v64
	v_and_b32_e32 v72, 0x7070707, v224
	v_perm_b32 v66, s2, v205, v66
	v_perm_b32 v72, s2, v205, v72
	v_and_or_b32 v66, v64, s4, v66
	v_and_or_b32 v64, v224, s4, v72
	v_perm_b32 v73, v64, v66, s33
	v_perm_b32 v76, v64, v66, s0
	v_perm_b32 v72, v64, v66, s5
	v_perm_b32 v64, v64, v66, s1
	v_pk_fma_f16 v66, v73, s59, v68 op_sel_hi:[1,0,1]
	v_pk_fma_f16 v68, v76, s59, v70 op_sel_hi:[1,0,1]
	s_add_u32 s66, s26, s64
	s_addc_u32 s67, s27, s65
	global_load_dwordx2 v[76:77], v121, s[66:67]
	v_alignbit_b32 v225, v65, v65, 4
	v_pk_fma_f16 v8, v64, s59, v8 op_sel_hi:[1,0,1]
	v_and_b32_e32 v64, 0x7070707, v65
	v_and_b32_e32 v70, 0x7070707, v225
	v_pk_fma_f16 v9, v72, s59, v9 op_sel_hi:[1,0,1]
	v_perm_b32 v64, s2, v205, v64
	v_perm_b32 v70, s2, v205, v70
	v_and_or_b32 v64, v65, s4, v64
	v_and_or_b32 v65, v225, s4, v70
	v_perm_b32 v70, v65, v64, s5
	v_perm_b32 v72, v65, v64, s33
	v_perm_b32 v73, v65, v64, s0
	v_perm_b32 v64, v65, v64, s1
	v_pk_fma_f16 v65, v70, s59, v67 op_sel_hi:[1,0,1]
	v_readlane_b32 s60, v120, 56
	s_waitcnt vmcnt(31)
	v_alignbit_b32 v224, v62, v62, 4
	v_pk_fma_f16 v67, v72, s59, v69 op_sel_hi:[1,0,1]
	v_pk_fma_f16 v69, v73, s59, v71 op_sel_hi:[1,0,1]
	v_pk_fma_f16 v7, v64, s59, v7 op_sel_hi:[1,0,1]
	v_and_b32_e32 v64, 0x7070707, v62
	v_and_b32_e32 v70, 0x7070707, v224
	v_perm_b32 v64, s2, v205, v64
	v_perm_b32 v70, s2, v205, v70
	v_and_or_b32 v64, v62, s4, v64
	v_and_or_b32 v62, v224, s4, v70
	v_perm_b32 v71, v62, v64, s33
	v_perm_b32 v72, v62, v64, s0
	v_perm_b32 v70, v62, v64, s5
	v_perm_b32 v62, v62, v64, s1
	v_pk_fma_f16 v64, v71, s60, v66 op_sel_hi:[1,0,1]
	v_pk_fma_f16 v66, v72, s60, v68 op_sel_hi:[1,0,1]
	s_add_u32 s66, s34, s64
	s_addc_u32 s67, s35, s65
	global_load_dwordx2 v[72:73], v121, s[66:67]
	v_alignbit_b32 v225, v63, v63, 4
	v_pk_fma_f16 v8, v62, s60, v8 op_sel_hi:[1,0,1]
	v_and_b32_e32 v62, 0x7070707, v63
	v_and_b32_e32 v68, 0x7070707, v225
	v_pk_fma_f16 v9, v70, s60, v9 op_sel_hi:[1,0,1]
	v_perm_b32 v62, s2, v205, v62
	v_perm_b32 v68, s2, v205, v68
	v_and_or_b32 v62, v63, s4, v62
	v_and_or_b32 v63, v225, s4, v68
	v_perm_b32 v68, v63, v62, s5
	v_perm_b32 v70, v63, v62, s33
	v_perm_b32 v71, v63, v62, s0
	v_perm_b32 v62, v63, v62, s1
	v_pk_fma_f16 v7, v62, s60, v7 op_sel_hi:[1,0,1]
	v_readlane_b32 s36, v120, 60
	s_waitcnt vmcnt(29)
	v_alignbit_b32 v224, v50, v50, 4
	v_pk_fma_f16 v63, v68, s60, v65 op_sel_hi:[1,0,1]
	v_pk_fma_f16 v65, v70, s60, v67 op_sel_hi:[1,0,1]
	v_pk_fma_f16 v67, v71, s60, v69 op_sel_hi:[1,0,1]
	s_add_u32 s66, s28, s64
	s_addc_u32 s67, s29, s65
	global_load_dwordx2 v[70:71], v121, s[66:67]
	v_and_b32_e32 v15, 0x7070707, v50
	v_and_b32_e32 v62, 0x7070707, v224
	v_perm_b32 v15, s2, v205, v15
	v_perm_b32 v62, s2, v205, v62
	v_and_or_b32 v15, v50, s4, v15
	v_and_or_b32 v50, v224, s4, v62
	v_perm_b32 v62, v50, v15, s5
	v_perm_b32 v68, v50, v15, s33
	v_perm_b32 v69, v50, v15, s0
	v_perm_b32 v15, v50, v15, s1
	v_pk_fma_f16 v105, v62, s36, v9 op_sel_hi:[1,0,1]
	v_alignbit_b32 v225, v51, v51, 4
	v_pk_fma_f16 v102, v15, s36, v8 op_sel_hi:[1,0,1]
	v_and_b32_e32 v8, 0x7070707, v51
	v_and_b32_e32 v9, 0x7070707, v225
	v_perm_b32 v8, s2, v205, v8
	v_perm_b32 v9, s2, v205, v9
	v_and_or_b32 v8, v51, s4, v8
	v_and_or_b32 v9, v225, s4, v9
	v_perm_b32 v15, v9, v8, s5
	v_perm_b32 v50, v9, v8, s33
	v_perm_b32 v51, v9, v8, s0
	v_perm_b32 v8, v9, v8, s1
	v_pk_fma_f16 v104, v68, s36, v64 op_sel_hi:[1,0,1]
	v_pk_fma_f16 v103, v69, s36, v66 op_sel_hi:[1,0,1]
	s_add_u32 s66, s38, s64
	s_addc_u32 s67, s39, s65
	global_load_dwordx2 v[68:69], v121, s[66:67]
	v_pk_fma_f16 v101, v15, s36, v63 op_sel_hi:[1,0,1]
	s_add_u32 s66, s52, s64
	s_addc_u32 s67, s53, s65
	global_load_dwordx2 v[62:63], v121, s[66:67]
	v_pk_fma_f16 v100, v50, s36, v65 op_sel_hi:[1,0,1]
	s_add_u32 s66, s50, s64
	s_addc_u32 s67, s51, s65
	global_load_dwordx2 v[64:65], v121, s[66:67]
	v_pk_fma_f16 v99, v51, s36, v67 op_sel_hi:[1,0,1]
	s_add_u32 s66, s30, s64
	s_addc_u32 s67, s31, s65
	global_load_dwordx2 v[66:67], v121, s[66:67]
	s_add_u32 s66, s54, s64
	s_addc_u32 s67, s55, s65
	global_load_dwordx2 v[50:51], v121, s[66:67]
	v_pk_fma_f16 v15, v8, s36, v7 op_sel_hi:[1,0,1]
	s_cmpk_eq_i32 s56, 0x90
	s_cbranch_scc0 .LBB0_770
	v_lshl_add_u64 v[94:95], v[2:3], 2, v[44:45]
	v_mov_b32_e32 v106, v208
	v_mov_b32_e32 v107, v209
	v_mov_b32_e32 v108, v210
	v_mov_b32_e32 v109, v211
	v_mov_b32_e32 v8, v212
	v_mov_b32_e32 v9, v213
	v_mov_b32_e32 v10, v214
	v_mov_b32_e32 v11, v215
	v_mov_b32_e32 v4, v216
	v_mov_b32_e32 v5, v217
	v_mov_b32_e32 v6, v218
	v_mov_b32_e32 v7, v219
	v_mov_b32_e32 v0, v220
	v_mov_b32_e32 v1, v221
	v_mov_b32_e32 v2, v222
	v_mov_b32_e32 v3, v223
	v_cvt_f32_f16_sdwa v13, v105 dst_sel:DWORD dst_unused:UNUSED_PAD src0_sel:WORD_1
	v_cvt_f32_f16_e32 v12, v105
	s_mov_b32 s12, 0x800000
	v_readlane_b32 s10, v255, 5
	v_readlane_b32 s11, v255, 6
	v_pk_add_f32 v[0:1], v[0:1], v[12:13]
	v_cvt_f32_f16_sdwa v13, v104 dst_sel:DWORD dst_unused:UNUSED_PAD src0_sel:WORD_1
	v_cvt_f32_f16_e32 v12, v104
	v_lshl_add_u64 v[48:49], v[48:49], 0, s[10:11]
	v_pk_add_f32 v[2:3], v[2:3], v[12:13]
	v_cvt_f32_f16_sdwa v13, v103 dst_sel:DWORD dst_unused:UNUSED_PAD src0_sel:WORD_1
	v_cvt_f32_f16_e32 v12, v103
	global_store_dwordx4 v[94:95], v[0:3], off
	v_pk_add_f32 v[4:5], v[4:5], v[12:13]
	v_cvt_f32_f16_sdwa v13, v102 dst_sel:DWORD dst_unused:UNUSED_PAD src0_sel:WORD_1
	v_cvt_f32_f16_e32 v12, v102
	v_mov_b32_e32 v102, v1
	v_mov_b32_e32 v103, v5
	v_pk_mul_f32 v[102:103], v[102:103], v[102:103]
	v_pk_add_f32 v[6:7], v[6:7], v[12:13]
	v_mov_b32_e32 v12, v0
	v_mov_b32_e32 v13, v4
	v_pk_fma_f32 v[12:13], v[12:13], v[12:13], v[102:103]
	v_mov_b32_e32 v102, v2
	v_mov_b32_e32 v103, v6
	v_pk_fma_f32 v[12:13], v[102:103], v[102:103], v[12:13]
	v_mov_b32_e32 v102, v3
	v_mov_b32_e32 v103, v7
	v_pk_fma_f32 v[102:103], v[102:103], v[102:103], v[12:13]
	v_cvt_f32_f16_sdwa v13, v101 dst_sel:DWORD dst_unused:UNUSED_PAD src0_sel:WORD_1
	v_cvt_f32_f16_e32 v12, v101
	v_cvt_f32_f16_sdwa v101, v15 dst_sel:DWORD dst_unused:UNUSED_PAD src0_sel:WORD_1
	global_store_dwordx4 v[94:95], v[4:7], off offset:16
	v_pk_add_f32 v[8:9], v[8:9], v[12:13]
	v_cvt_f32_f16_sdwa v13, v100 dst_sel:DWORD dst_unused:UNUSED_PAD src0_sel:WORD_1
	v_cvt_f32_f16_e32 v12, v100
	v_cvt_f32_f16_e32 v100, v15
	v_pk_add_f32 v[10:11], v[10:11], v[12:13]
	v_cvt_f32_f16_sdwa v13, v99 dst_sel:DWORD dst_unused:UNUSED_PAD src0_sel:WORD_1
	v_cvt_f32_f16_e32 v12, v99
	v_pk_add_f32 v[14:15], v[108:109], v[100:101]
	v_mov_b32_e32 v100, v9
	global_store_dwordx4 v[94:95], v[8:11], off offset:32
	v_pk_add_f32 v[12:13], v[106:107], v[12:13]
	global_store_dwordx4 v[94:95], v[12:15], off offset:48
	v_mov_b32_e32 v101, v13
	v_mov_b32_e32 v94, v8
	v_mov_b32_e32 v95, v12
	v_pk_mul_f32 v[100:101], v[100:101], v[100:101]
	v_add_f32_e32 v99, v102, v103
	v_pk_fma_f32 v[94:95], v[94:95], v[94:95], v[100:101]
	v_mov_b32_e32 v100, v10
	v_mov_b32_e32 v101, v14
	v_pk_fma_f32 v[94:95], v[100:101], v[100:101], v[94:95]
	v_mov_b32_e32 v100, v11
	v_mov_b32_e32 v101, v15
	v_pk_fma_f32 v[94:95], v[100:101], v[100:101], v[94:95]
	v_mov_b64_e32 v[100:101], v[136:137]
	v_mov_b64_e32 v[102:103], v[138:139]
	v_mov_b64_e32 v[104:105], v[132:133]
	v_mov_b64_e32 v[106:107], v[134:135]
	v_mov_b64_e32 v[108:109], v[128:129]
	v_mov_b64_e32 v[110:111], v[130:131]
	v_mov_b64_e32 v[112:113], v[124:125]
	v_mov_b64_e32 v[114:115], v[126:127]
	v_add_f32_e32 v94, v99, v94
	v_add_f32_e32 v94, v94, v95
	v_mov_b32_e32 v95, v94
	s_nop 1
	v_permlane32_swap_b32 v95, v94
	s_waitcnt lgkmcnt(0)
	v_add_f32_e32 v94, v94, v95
	v_mov_b32_e32 v95, v94
	s_nop 1
	v_permlane16_swap_b32 v95, v94
	s_waitcnt lgkmcnt(0)
	v_add_f32_e32 v94, v94, v95
	s_nop 1
	v_mov_b32_dpp v95, v94 row_ror:8 row_mask:0xf bank_mask:0xf
	s_waitcnt lgkmcnt(0)
	v_add_f32_e32 v94, v94, v95
	s_nop 1
	v_mov_b32_dpp v95, v94 row_half_mirror row_mask:0xf bank_mask:0xf
	s_nop 1
	v_mov_b32_dpp v95, v95 quad_perm:[3,2,1,0] row_mask:0xf bank_mask:0xf
	s_waitcnt lgkmcnt(0)
	v_add_f32_e32 v94, v94, v95
	s_nop 1
	v_mov_b32_dpp v95, v94 quad_perm:[2,3,0,1] row_mask:0xf bank_mask:0xf
	s_waitcnt lgkmcnt(0)
	v_add_f32_e32 v94, v94, v95
	s_nop 1
	v_mov_b32_dpp v95, v94 quad_perm:[1,0,3,2] row_mask:0xf bank_mask:0xf
	s_waitcnt lgkmcnt(0)
	v_add_f32_e32 v94, v94, v95
	v_fmamk_f32 v94, v94, 0x3a800000, v191
	v_cmp_gt_f32_e32 vcc, s12, v94
	v_mul_f32_e32 v95, 0x4b800000, v94
	s_nop 0
	v_cndmask_b32_e32 v94, v94, v95, vcc
	v_rsq_f32_e32 v94, v94
	s_nop 0
	v_mul_f32_e32 v95, 0x45800000, v94
	v_cndmask_b32_e32 v94, v94, v95, vcc
	v_pk_mul_f32 v[0:1], v[0:1], v[94:95] op_sel_hi:[1,0]
	v_pk_mul_f32 v[2:3], v[2:3], v[94:95] op_sel_hi:[1,0]
	v_pk_mul_f32 v[0:1], v[112:113], v[0:1]
	v_pk_mul_f32 v[2:3], v[114:115], v[2:3]
	v_cvt_pk_bf16_f32 v0, v0, v1
	v_cvt_pk_bf16_f32 v1, v2, v3
	v_pk_mul_f32 v[2:3], v[4:5], v[94:95] op_sel_hi:[1,0]
	v_pk_mul_f32 v[4:5], v[6:7], v[94:95] op_sel_hi:[1,0]
	v_pk_mul_f32 v[2:3], v[108:109], v[2:3]
	v_pk_mul_f32 v[4:5], v[110:111], v[4:5]
	v_cvt_pk_bf16_f32 v2, v2, v3
	v_cvt_pk_bf16_f32 v3, v4, v5
	v_pk_mul_f32 v[4:5], v[8:9], v[94:95] op_sel_hi:[1,0]
	v_pk_mul_f32 v[6:7], v[10:11], v[94:95] op_sel_hi:[1,0]
	v_pk_mul_f32 v[4:5], v[104:105], v[4:5]
	v_pk_mul_f32 v[6:7], v[6:7], v[106:107]
	v_cvt_pk_bf16_f32 v4, v4, v5
	v_cvt_pk_bf16_f32 v5, v6, v7
	v_pk_mul_f32 v[6:7], v[12:13], v[94:95] op_sel_hi:[1,0]
	v_pk_mul_f32 v[8:9], v[14:15], v[94:95] op_sel_hi:[1,0]
	v_pk_mul_f32 v[6:7], v[6:7], v[100:101]
	v_pk_mul_f32 v[8:9], v[8:9], v[102:103]
	v_cvt_pk_bf16_f32 v6, v6, v7
	v_cvt_pk_bf16_f32 v7, v8, v9
	global_store_dwordx4 v[74:75], v[0:3], off
	global_store_dwordx4 v[74:75], v[4:7], off offset:16
	s_nop 0
	v_mov_b32_e32 v0, v98
	s_andn2_b64 exec, exec, s[8:9]
	s_cbranch_execnz .LBB0_769
